# baseline (speedup 1.0000x reference)
.Lmy_proj_noprio:
	s_load_dwordx4 s[4:7], s[0:1], 0x20
	s_load_dwordx2 s[12:13], s[0:1], 0x30
	v_and_b32_e32 v73, 63, v0
	v_and_b32_e32 v1, 31, v0
	v_lshrrev_b32_e32 v76, 6, v0
	v_bfe_u32 v77, v0, 5, 1
	v_or_b32_e32 v45, 0x200, v0
	v_or_b32_e32 v46, 0x600, v0
	v_or_b32_e32 v47, 0xa00, v0
	v_or_b32_e32 v48, 0xe00, v0
	v_lshlrev_b32_e32 v34, 15, v76
	v_mov_b32_e32 v35, v71
	v_lshl_add_u64 v[34:35], s[8:9], 0, v[34:35]
	v_lshlrev_b32_e32 v36, 4, v73
	v_mov_b32_e32 v37, v71
	v_lshl_add_u64 v[68:69], v[34:35], 0, v[36:37]
	s_movk_i32 s0, 0x5000
	v_add_co_u32_e32 v38, vcc, s0, v68
	s_movk_i32 s0, 0x4000
	s_nop 0
	v_addc_co_u32_e32 v39, vcc, 0, v69, vcc
	global_load_dwordx4 v[34:37], v[68:69], off
	global_load_dwordx4 v[78:81], v[38:39], off offset:-4096
	v_add_co_u32_e32 v40, vcc, s0, v68
	s_nop 1
	v_addc_co_u32_e32 v41, vcc, 0, v69, vcc
	global_load_dwordx4 v[82:85], v[68:69], off offset:1024
	global_load_dwordx4 v[86:89], v[40:41], off offset:1024
	global_load_dwordx4 v[90:93], v[68:69], off offset:2048
	global_load_dwordx4 v[94:97], v[40:41], off offset:2048
	global_load_dwordx4 v[98:101], v[68:69], off offset:3072
	global_load_dwordx4 v[102:105], v[40:41], off offset:3072
	v_add_co_u32_e32 v74, vcc, s14, v68
	s_movk_i32 s0, 0x1000
	s_nop 0
	v_addc_co_u32_e32 v75, vcc, 0, v69, vcc
	global_load_dwordx4 v[106:109], v[74:75], off offset:-4096
	global_load_dwordx4 v[110:113], v[38:39], off
	v_add_co_u32_e32 v40, vcc, s0, v68
	s_nop 1
	v_addc_co_u32_e32 v41, vcc, 0, v69, vcc
	global_load_dwordx4 v[114:117], v[40:41], off offset:1024
	global_load_dwordx4 v[118:121], v[38:39], off offset:1024
	global_load_dwordx4 v[122:125], v[40:41], off offset:2048
	global_load_dwordx4 v[126:129], v[38:39], off offset:2048
	global_load_dwordx4 v[130:133], v[40:41], off offset:3072
	global_load_dwordx4 v[134:137], v[38:39], off offset:3072
	v_lshlrev_b32_e32 v38, 3, v0
	v_and_b32_e32 v38, 0x1f8, v38
	v_add_u32_e32 v38, 0, v38
	s_movk_i32 s0, 0x210
	s_waitcnt vmcnt(17)
	v_cvt_pk_f16_f32 v29, v28, v29
	v_cvt_pk_f16_f32 v28, v26, v27
	v_mad_u32_u24 v26, v76, s0, v38
	ds_write_b64 v26, v[28:29]
	v_lshrrev_b32_e32 v26, 6, v45
	v_cvt_pk_f16_f32 v5, v4, v5
	v_cvt_pk_f16_f32 v4, v2, v3
	v_mad_u32_u24 v2, v26, s0, v38
	ds_write_b64 v2, v[4:5]
	v_lshrrev_b32_e32 v4, 6, v42
	v_cvt_pk_f16_f32 v3, v8, v9
	v_cvt_pk_f16_f32 v2, v6, v7
	v_mad_u32_u24 v4, v4, s0, v38
	ds_write_b64 v4, v[2:3]
	v_lshrrev_b32_e32 v4, 6, v46
	v_cvt_pk_f16_f32 v3, v12, v13
	v_cvt_pk_f16_f32 v2, v10, v11
	v_mad_u32_u24 v4, v4, s0, v38
	ds_write_b64 v4, v[2:3]
	v_lshrrev_b32_e32 v4, 6, v43
	v_cvt_pk_f16_f32 v3, v16, v17
	v_cvt_pk_f16_f32 v2, v14, v15
	v_mad_u32_u24 v4, v4, s0, v38
	ds_write_b64 v4, v[2:3]
	v_lshrrev_b32_e32 v4, 6, v47
	v_cvt_pk_f16_f32 v3, v20, v21
	v_cvt_pk_f16_f32 v2, v18, v19
	v_mad_u32_u24 v4, v4, s0, v38
	ds_write_b64 v4, v[2:3]
	v_lshrrev_b32_e32 v4, 6, v44
	v_cvt_pk_f16_f32 v3, v24, v25
	v_cvt_pk_f16_f32 v2, v22, v23
	v_mad_u32_u24 v4, v4, s0, v38
	ds_write_b64 v4, v[2:3]
	v_lshrrev_b32_e32 v4, 6, v48
	s_waitcnt vmcnt(16)
	v_cvt_pk_f16_f32 v3, v32, v33
	v_cvt_pk_f16_f32 v2, v30, v31
	v_mad_u32_u24 v4, v4, s0, v38
	ds_write_b64 v4, v[2:3]
	v_mul_u32_u24_e32 v2, 0x210, v1
	v_lshlrev_b32_e32 v66, 4, v77
	v_add3_u32 v67, 0, v2, v66
	s_waitcnt lgkmcnt(0)
	s_barrier
	ds_read_b128 v[2:5], v67
	ds_read_b128 v[138:141], v67 offset:32
	ds_read_b128 v[6:9], v67 offset:16896
	ds_read_b128 v[142:145], v67 offset:16928
	s_movk_i32 s0, 0x7000
	v_add_co_u32_e32 v166, vcc, s0, v68
	s_waitcnt vmcnt(15) lgkmcnt(3)
	v_mfma_f32_32x32x16_f16 v[50:65], v[34:37], v[2:5], 0
	v_addc_co_u32_e32 v167, vcc, 0, v69, vcc
	global_load_dwordx4 v[146:149], v[74:75], off
	global_load_dwordx4 v[150:153], v[166:167], off offset:-4096
	ds_read_b128 v[154:157], v67 offset:64
	ds_read_b128 v[158:161], v67 offset:16960
	v_add_co_u32_e32 v168, vcc, s3, v68
	s_waitcnt lgkmcnt(3)
	v_mfma_f32_32x32x16_f16 v[34:49], v[34:37], v[6:9], 0
	v_addc_co_u32_e32 v169, vcc, 0, v69, vcc
	s_waitcnt vmcnt(16)
	v_mfma_f32_32x32x16_f16 v[18:33], v[78:81], v[2:5], 0
	v_mfma_f32_32x32x16_f16 v[2:17], v[78:81], v[6:9], 0
	s_waitcnt vmcnt(15)
	v_mfma_f32_32x32x16_f16 v[50:65], v[82:85], v[138:141], v[50:65]
	s_waitcnt lgkmcnt(2)
	v_mfma_f32_32x32x16_f16 v[34:49], v[82:85], v[142:145], v[34:49]
	global_load_dwordx4 v[78:81], v[74:75], off offset:1024
	global_load_dwordx4 v[82:85], v[168:169], off offset:1024
	s_waitcnt vmcnt(16)
	v_mfma_f32_32x32x16_f16 v[2:17], v[86:89], v[142:145], v[2:17]
	v_mfma_f32_32x32x16_f16 v[18:33], v[86:89], v[138:141], v[18:33]
	ds_read_b128 v[138:141], v67 offset:96
	ds_read_b128 v[162:165], v67 offset:16992
	s_waitcnt vmcnt(15) lgkmcnt(3)
	v_mfma_f32_32x32x16_f16 v[50:65], v[90:93], v[154:157], v[50:65]
	s_waitcnt lgkmcnt(2)
	v_mfma_f32_32x32x16_f16 v[34:49], v[90:93], v[158:161], v[34:49]
	global_load_dwordx4 v[86:89], v[74:75], off offset:2048
	global_load_dwordx4 v[90:93], v[168:169], off offset:2048
	s_waitcnt vmcnt(16)
	v_mfma_f32_32x32x16_f16 v[2:17], v[94:97], v[158:161], v[2:17]
	v_mfma_f32_32x32x16_f16 v[18:33], v[94:97], v[154:157], v[18:33]
	ds_read_b128 v[142:145], v67 offset:128
	ds_read_b128 v[154:157], v67 offset:17024
	s_waitcnt vmcnt(15) lgkmcnt(3)
	v_mfma_f32_32x32x16_f16 v[50:65], v[98:101], v[138:141], v[50:65]
	s_waitcnt lgkmcnt(2)
	v_mfma_f32_32x32x16_f16 v[34:49], v[98:101], v[162:165], v[34:49]
	global_load_dwordx4 v[94:97], v[74:75], off offset:3072
	global_load_dwordx4 v[98:101], v[168:169], off offset:3072
	s_waitcnt vmcnt(16)
	v_mfma_f32_32x32x16_f16 v[2:17], v[102:105], v[162:165], v[2:17]
	v_mfma_f32_32x32x16_f16 v[18:33], v[102:105], v[138:141], v[18:33]
	ds_read_b128 v[138:141], v67 offset:160
	ds_read_b128 v[158:161], v67 offset:17056
	s_movk_i32 s0, 0x3000
	v_add_co_u32_e32 v68, vcc, s0, v68
	s_waitcnt vmcnt(15) lgkmcnt(3)
	v_mfma_f32_32x32x16_f16 v[50:65], v[106:109], v[142:145], v[50:65]
	v_addc_co_u32_e32 v69, vcc, 0, v69, vcc
	s_waitcnt lgkmcnt(2)
	v_mfma_f32_32x32x16_f16 v[34:49], v[106:109], v[154:157], v[34:49]
	global_load_dwordx4 v[102:105], v[68:69], off
	global_load_dwordx4 v[106:109], v[166:167], off
	s_waitcnt vmcnt(16)
	v_mfma_f32_32x32x16_f16 v[2:17], v[110:113], v[154:157], v[2:17]
	v_mfma_f32_32x32x16_f16 v[18:33], v[110:113], v[142:145], v[18:33]
	ds_read_b128 v[142:145], v67 offset:192
	ds_read_b128 v[162:165], v67 offset:17088
	s_waitcnt vmcnt(15) lgkmcnt(3)
	v_mfma_f32_32x32x16_f16 v[50:65], v[114:117], v[138:141], v[50:65]
	s_waitcnt lgkmcnt(2)
	v_mfma_f32_32x32x16_f16 v[34:49], v[114:117], v[158:161], v[34:49]
	global_load_dwordx4 v[110:113], v[68:69], off offset:1024
	global_load_dwordx4 v[114:117], v[166:167], off offset:1024
	s_waitcnt vmcnt(16)
	v_mfma_f32_32x32x16_f16 v[2:17], v[118:121], v[158:161], v[2:17]
	v_mfma_f32_32x32x16_f16 v[18:33], v[118:121], v[138:141], v[18:33]
	ds_read_b128 v[138:141], v67 offset:224
	ds_read_b128 v[154:157], v67 offset:17120
	s_waitcnt vmcnt(15) lgkmcnt(3)
	v_mfma_f32_32x32x16_f16 v[50:65], v[122:125], v[142:145], v[50:65]
	s_waitcnt lgkmcnt(2)
	v_mfma_f32_32x32x16_f16 v[34:49], v[122:125], v[162:165], v[34:49]
	global_load_dwordx4 v[118:121], v[68:69], off offset:2048
	global_load_dwordx4 v[122:125], v[166:167], off offset:2048
	s_waitcnt vmcnt(16)
	v_mfma_f32_32x32x16_f16 v[2:17], v[126:129], v[162:165], v[2:17]
	v_mfma_f32_32x32x16_f16 v[18:33], v[126:129], v[142:145], v[18:33]
	ds_read_b128 v[142:145], v67 offset:256
	ds_read_b128 v[158:161], v67 offset:17152
	s_waitcnt vmcnt(15) lgkmcnt(3)
	v_mfma_f32_32x32x16_f16 v[50:65], v[130:133], v[138:141], v[50:65]
	s_waitcnt lgkmcnt(2)
	v_mfma_f32_32x32x16_f16 v[34:49], v[130:133], v[154:157], v[34:49]
	global_load_dwordx4 v[126:129], v[68:69], off offset:3072
	global_load_dwordx4 v[130:133], v[166:167], off offset:3072
	s_waitcnt vmcnt(16)
	v_mfma_f32_32x32x16_f16 v[2:17], v[134:137], v[154:157], v[2:17]
	v_mfma_f32_32x32x16_f16 v[18:33], v[134:137], v[138:141], v[18:33]
	ds_read_b128 v[138:141], v67 offset:288
	ds_read_b128 v[162:165], v67 offset:17184
	s_waitcnt vmcnt(14) lgkmcnt(2)
	v_mfma_f32_32x32x16_f16 v[2:17], v[150:153], v[158:161], v[2:17]
	v_mfma_f32_32x32x16_f16 v[50:65], v[146:149], v[142:145], v[50:65]
	v_mfma_f32_32x32x16_f16 v[18:33], v[150:153], v[142:145], v[18:33]
	ds_read_b128 v[134:137], v67 offset:320
	ds_read_b128 v[142:145], v67 offset:17216
	v_mfma_f32_32x32x16_f16 v[34:49], v[146:149], v[158:161], v[34:49]
	s_waitcnt vmcnt(12) lgkmcnt(2)
	v_mfma_f32_32x32x16_f16 v[2:17], v[82:85], v[162:165], v[2:17]
	v_mfma_f32_32x32x16_f16 v[50:65], v[78:81], v[138:141], v[50:65]
	v_mfma_f32_32x32x16_f16 v[34:49], v[78:81], v[162:165], v[34:49]
	v_mfma_f32_32x32x16_f16 v[18:33], v[82:85], v[138:141], v[18:33]
	ds_read_b128 v[78:81], v67 offset:352
	ds_read_b128 v[138:141], v67 offset:17248
	s_waitcnt vmcnt(10) lgkmcnt(2)
	v_mfma_f32_32x32x16_f16 v[2:17], v[90:93], v[142:145], v[2:17]
	v_mfma_f32_32x32x16_f16 v[50:65], v[86:89], v[134:137], v[50:65]
	v_mfma_f32_32x32x16_f16 v[34:49], v[86:89], v[142:145], v[34:49]
	ds_read_b128 v[82:85], v67 offset:384
	ds_read_b128 v[86:89], v67 offset:17280
	v_mfma_f32_32x32x16_f16 v[18:33], v[90:93], v[134:137], v[18:33]
	s_waitcnt vmcnt(8) lgkmcnt(2)
	v_mfma_f32_32x32x16_f16 v[2:17], v[98:101], v[138:141], v[2:17]
	v_mfma_f32_32x32x16_f16 v[50:65], v[94:97], v[78:81], v[50:65]
	v_mfma_f32_32x32x16_f16 v[18:33], v[98:101], v[78:81], v[18:33]
	ds_read_b128 v[78:81], v67 offset:416
	ds_read_b128 v[90:93], v67 offset:17312
	v_mfma_f32_32x32x16_f16 v[34:49], v[94:97], v[138:141], v[34:49]
	s_waitcnt vmcnt(6) lgkmcnt(2)
	v_mfma_f32_32x32x16_f16 v[2:17], v[106:109], v[86:89], v[2:17]
	v_mfma_f32_32x32x16_f16 v[50:65], v[102:105], v[82:85], v[50:65]
	v_mfma_f32_32x32x16_f16 v[18:33], v[106:109], v[82:85], v[18:33]
	ds_read_b128 v[82:85], v67 offset:448
	ds_read_b128 v[94:97], v67 offset:17344
	v_mfma_f32_32x32x16_f16 v[34:49], v[102:105], v[86:89], v[34:49]
	s_waitcnt vmcnt(4) lgkmcnt(2)
	v_mfma_f32_32x32x16_f16 v[2:17], v[114:117], v[90:93], v[2:17]
	v_mfma_f32_32x32x16_f16 v[50:65], v[110:113], v[78:81], v[50:65]
	v_mfma_f32_32x32x16_f16 v[18:33], v[114:117], v[78:81], v[18:33]
	ds_read_b128 v[78:81], v67 offset:480
	ds_read_b128 v[86:89], v67 offset:17376
	v_mfma_f32_32x32x16_f16 v[34:49], v[110:113], v[90:93], v[34:49]
	s_waitcnt vmcnt(2) lgkmcnt(2)
	v_mfma_f32_32x32x16_f16 v[2:17], v[122:125], v[94:97], v[2:17]
	v_mfma_f32_32x32x16_f16 v[50:65], v[118:121], v[82:85], v[50:65]
	v_mfma_f32_32x32x16_f16 v[34:49], v[118:121], v[94:97], v[34:49]
	v_mfma_f32_32x32x16_f16 v[18:33], v[122:125], v[82:85], v[18:33]
	s_waitcnt vmcnt(0) lgkmcnt(0)
	v_mfma_f32_32x32x16_f16 v[2:17], v[130:133], v[86:89], v[2:17]
	v_mfma_f32_32x32x16_f16 v[50:65], v[126:129], v[78:81], v[50:65]
	v_mfma_f32_32x32x16_f16 v[34:49], v[126:129], v[86:89], v[34:49]
	v_mfma_f32_32x32x16_f16 v[18:33], v[130:133], v[78:81], v[18:33]
	v_and_b32_e32 v98, 0x1c0, v0
	v_and_b32_e32 v67, 0xc0, v0
	v_lshlrev_b32_e32 v74, 2, v98
	v_mov_b32_e32 v75, v71
	s_movk_i32 s0, 0xfc00
	s_movk_i32 s3, 0x100
	v_lshlrev_b32_e32 v68, 2, v67
	v_mov_b32_e32 v69, v71
	v_lshl_add_u64 v[74:75], s[4:5], 0, v[74:75]
	s_mov_b32 s1, -1
	v_lshl_add_u64 v[68:69], s[10:11], 0, v[68:69]
	v_lshl_add_u64 v[74:75], v[74:75], 0, s[0:1]
	v_mov_b32_e32 v67, 0x3ed96d27
	v_cmp_gt_u32_e32 vcc, s3, v0
	s_nop 1
	v_cndmask_b32_e32 v72, 1.0, v67, vcc
	v_cndmask_b32_e32 v69, v75, v69, vcc
	v_cndmask_b32_e32 v68, v74, v68, vcc
	v_mov_b32_e32 v67, v71
	v_lshl_add_u64 v[74:75], v[68:69], 0, v[66:67]
	global_load_dwordx4 v[66:69], v[74:75], off
	global_load_dwordx4 v[78:81], v[74:75], off offset:32
	global_load_dwordx4 v[82:85], v[74:75], off offset:64
	global_load_dwordx4 v[86:89], v[74:75], off offset:96
	global_load_dwordx4 v[90:93], v[74:75], off offset:128
	global_load_dwordx4 v[94:97], v[74:75], off offset:160
	s_movk_i32 s0, 0x90
	v_mad_u32_u24 v71, v98, s0, 0
	global_load_dwordx4 v[98:101], v[74:75], off offset:192
	global_load_dwordx4 v[102:105], v[74:75], off offset:224
	v_lshlrev_b32_e32 v77, 3, v77
	v_mul_u32_u24_e32 v1, 0x90, v1
	v_add3_u32 v77, v71, v77, v1
	s_movk_i32 s0, 0xff
	v_add_u32_e32 v106, 0x1000, v77
	v_cmp_lt_u32_e64 s[0:1], s0, v0
	s_lshr_b32 s3, s2, 3
	s_and_b32 s3, s3, 0x3ffc
	s_lshl_b32 s2, s2, 13
	s_and_b32 s2, s2, 0x3e000
	s_barrier
	s_waitcnt vmcnt(7)
	v_pk_add_f32 v[50:51], v[66:67], v[50:51]
	v_pk_add_f32 v[52:53], v[68:69], v[52:53]
	s_waitcnt vmcnt(6)
	v_pk_add_f32 v[54:55], v[78:79], v[54:55]
	v_pk_add_f32 v[56:57], v[80:81], v[56:57]
	s_waitcnt vmcnt(3)
	v_pk_add_f32 v[18:19], v[90:91], v[18:19]
	v_pk_add_f32 v[20:21], v[92:93], v[20:21]
	v_pk_add_f32 v[2:3], v[90:91], v[2:3]
	v_pk_add_f32 v[4:5], v[92:93], v[4:5]
	v_pk_mul_f32 v[18:19], v[72:73], v[18:19] op_sel_hi:[0,1]
	v_pk_mul_f32 v[20:21], v[72:73], v[20:21] op_sel_hi:[0,1]
	v_pk_mul_f32 v[2:3], v[72:73], v[2:3] op_sel_hi:[0,1]
	v_pk_mul_f32 v[4:5], v[72:73], v[4:5] op_sel_hi:[0,1]
	v_cvt_pk_f16_f32 v18, v18, v19
	v_cvt_pk_f16_f32 v19, v20, v21
	v_cvt_pk_f16_f32 v2, v2, v3
	v_cvt_pk_f16_f32 v3, v4, v5
	s_waitcnt vmcnt(2)
	v_pk_add_f32 v[4:5], v[94:95], v[22:23]
	v_pk_add_f32 v[20:21], v[96:97], v[24:25]
	v_pk_add_f32 v[58:59], v[82:83], v[58:59]
	v_pk_add_f32 v[60:61], v[84:85], v[60:61]
	v_pk_add_f32 v[62:63], v[86:87], v[62:63]
	v_pk_add_f32 v[64:65], v[88:89], v[64:65]
	v_pk_add_f32 v[34:35], v[66:67], v[34:35]
	v_pk_add_f32 v[36:37], v[68:69], v[36:37]
	v_pk_add_f32 v[38:39], v[78:79], v[38:39]
	v_pk_add_f32 v[40:41], v[80:81], v[40:41]
	v_pk_mul_f32 v[50:51], v[72:73], v[50:51] op_sel_hi:[0,1]
	v_pk_mul_f32 v[52:53], v[72:73], v[52:53] op_sel_hi:[0,1]
	v_pk_mul_f32 v[54:55], v[72:73], v[54:55] op_sel_hi:[0,1]
	v_pk_mul_f32 v[56:57], v[72:73], v[56:57] op_sel_hi:[0,1]
	v_pk_mul_f32 v[4:5], v[72:73], v[4:5] op_sel_hi:[0,1]
	v_pk_mul_f32 v[20:21], v[72:73], v[20:21] op_sel_hi:[0,1]
	v_pk_mul_f32 v[34:35], v[72:73], v[34:35] op_sel_hi:[0,1]
	v_pk_mul_f32 v[36:37], v[72:73], v[36:37] op_sel_hi:[0,1]
	v_pk_mul_f32 v[38:39], v[72:73], v[38:39] op_sel_hi:[0,1]
	v_pk_mul_f32 v[40:41], v[72:73], v[40:41] op_sel_hi:[0,1]
	v_pk_mul_f32 v[58:59], v[72:73], v[58:59] op_sel_hi:[0,1]
	v_pk_mul_f32 v[60:61], v[72:73], v[60:61] op_sel_hi:[0,1]
	v_pk_mul_f32 v[62:63], v[72:73], v[62:63] op_sel_hi:[0,1]
	v_pk_mul_f32 v[64:65], v[72:73], v[64:65] op_sel_hi:[0,1]
	v_cvt_pk_f16_f32 v50, v50, v51
	v_cvt_pk_f16_f32 v51, v52, v53
	v_cvt_pk_f16_f32 v52, v54, v55
	v_cvt_pk_f16_f32 v53, v56, v57
	v_cvt_pk_f16_f32 v4, v4, v5
	v_cvt_pk_f16_f32 v5, v20, v21
	v_cvt_pk_f16_f32 v34, v34, v35
	v_cvt_pk_f16_f32 v35, v36, v37
	v_cvt_pk_f16_f32 v36, v38, v39
	v_cvt_pk_f16_f32 v37, v40, v41
	v_cvt_pk_f16_f32 v38, v58, v59
	v_cvt_pk_f16_f32 v39, v60, v61
	v_cvt_pk_f16_f32 v40, v62, v63
	v_cvt_pk_f16_f32 v41, v64, v65
	ds_write2_b64 v77, v[50:51], v[52:53] offset1:2
	ds_write2_b64 v106, v[34:35], v[36:37] offset0:64 offset1:66
	ds_write2_b64 v77, v[38:39], v[40:41] offset0:4 offset1:6
	ds_write2_b64 v77, v[18:19], v[4:5] offset0:8 offset1:10
	v_pk_add_f32 v[0:1], v[94:95], v[6:7]
	v_pk_add_f32 v[4:5], v[96:97], v[8:9]
	v_pk_mul_f32 v[0:1], v[72:73], v[0:1] op_sel_hi:[0,1]
	v_pk_mul_f32 v[4:5], v[72:73], v[4:5] op_sel_hi:[0,1]
	v_cvt_pk_f16_f32 v0, v0, v1
	v_cvt_pk_f16_f32 v1, v4, v5
	ds_write2_b64 v106, v[2:3], v[0:1] offset0:72 offset1:74
	s_waitcnt vmcnt(1)
	v_pk_add_f32 v[0:1], v[98:99], v[26:27]
	v_pk_add_f32 v[2:3], v[100:101], v[28:29]
	v_pk_mul_f32 v[0:1], v[72:73], v[0:1] op_sel_hi:[0,1]
	v_pk_mul_f32 v[2:3], v[72:73], v[2:3] op_sel_hi:[0,1]
	v_cvt_pk_f16_f32 v0, v0, v1
	v_cvt_pk_f16_f32 v1, v2, v3
	v_pk_add_f32 v[2:3], v[98:99], v[10:11]
	v_pk_add_f32 v[4:5], v[100:101], v[12:13]
	v_pk_mul_f32 v[2:3], v[72:73], v[2:3] op_sel_hi:[0,1]
	v_pk_mul_f32 v[4:5], v[72:73], v[4:5] op_sel_hi:[0,1]
	v_cvt_pk_f16_f32 v2, v2, v3
	v_cvt_pk_f16_f32 v3, v4, v5
	s_waitcnt vmcnt(0)
	v_pk_add_f32 v[4:5], v[102:103], v[30:31]
	v_pk_add_f32 v[6:7], v[104:105], v[32:33]
	v_pk_mul_f32 v[4:5], v[72:73], v[4:5] op_sel_hi:[0,1]
	v_pk_mul_f32 v[6:7], v[72:73], v[6:7] op_sel_hi:[0,1]
	v_cvt_pk_f16_f32 v4, v4, v5
	v_cvt_pk_f16_f32 v5, v6, v7
	ds_write2_b64 v77, v[0:1], v[4:5] offset0:12 offset1:14
	v_pk_add_f32 v[0:1], v[102:103], v[14:15]
	v_pk_add_f32 v[4:5], v[104:105], v[16:17]
	v_pk_mul_f32 v[0:1], v[72:73], v[0:1] op_sel_hi:[0,1]
	v_pk_mul_f32 v[4:5], v[72:73], v[4:5] op_sel_hi:[0,1]
	v_cvt_pk_f16_f32 v0, v0, v1
	v_cvt_pk_f16_f32 v1, v4, v5
	ds_write2_b64 v106, v[2:3], v[0:1] offset0:76 offset1:78
	v_mov_b32_e32 v0, s12
	v_mov_b32_e32 v1, s6
	v_pk_add_f32 v[42:43], v[82:83], v[42:43]
	v_pk_add_f32 v[44:45], v[84:85], v[44:45]
	v_pk_add_f32 v[46:47], v[86:87], v[46:47]
	v_pk_add_f32 v[48:49], v[88:89], v[48:49]
	v_cndmask_b32_e32 v0, v0, v1, vcc
	v_mov_b32_e32 v1, s13
	v_mov_b32_e32 v2, s7
	v_and_or_b32 v4, v76, 3, s3
	v_pk_mul_f32 v[42:43], v[72:73], v[42:43] op_sel_hi:[0,1]
	v_pk_mul_f32 v[44:45], v[72:73], v[44:45] op_sel_hi:[0,1]
	v_pk_mul_f32 v[46:47], v[72:73], v[46:47] op_sel_hi:[0,1]
	v_pk_mul_f32 v[48:49], v[72:73], v[48:49] op_sel_hi:[0,1]
	v_cndmask_b32_e32 v1, v1, v2, vcc
	v_lshl_or_b32 v4, v4, 18, s2
	v_cvt_pk_f16_f32 v42, v42, v43
	v_cvt_pk_f16_f32 v43, v44, v45
	v_cvt_pk_f16_f32 v44, v46, v47
	v_cvt_pk_f16_f32 v45, v48, v49
	v_and_b32_e32 v1, 0xffff, v1
	v_mov_b32_e32 v2, 0x800000
	v_mov_b32_e32 v3, 0x20000
	v_lshl_or_b32 v8, v73, 4, v4
	ds_write2_b64 v106, v[42:43], v[44:45] offset0:68 offset1:70
	s_and_saveexec_b64 s[2:3], s[0:1]
	s_xor_b64 s[2:3], exec, s[2:3]
	s_cbranch_execz .LBB1_18
	v_lshrrev_b32_e32 v4, 2, v73
	v_mul_u32_u24_e32 v4, 0x90, v4
	v_and_b32_e32 v5, 48, v70
	v_add3_u32 v9, v71, v4, v5
	ds_read_b128 v[4:7], v9
	s_mov_b64 s[8:9], exec
